# v7 + P4 retention units: the r_prev tile wait no longer drains the next unit's prefetch (counted waits, drain only when there is no next unit)
# speedup vs baseline: 1.0169x; 1.0169x over previous
.LBB0_570:
	s_and_b32 s88, s2, 7
	v_cvt_f32_ubyte0_e32 v66, s88
	v_sub_f32_e32 v82, 0xc0a00000, v66
	s_lshl_b32 s0, s2, 4
	v_cmp_gt_f32_e64 s[74:75], s89, v82
	s_and_b64 s[36:37], s[74:75], exec
	s_cselect_b32 s36, 0xffffffc0, 0
	s_and_b32 s0, s0, 0xffffff80
	v_add_u32_e32 v66, v1, v152
	v_add_u32_e32 v67, v1, v153
	v_add_u32_e32 v146, s0, v155
	ds_write_b128 v66, v[2:5]
	ds_write_b16 v192, v6 offset:34816
	ds_write_b16_d16_hi v192, v6 offset:35088
	ds_write_b16 v192, v7 offset:35360
	ds_write_b16_d16_hi v192, v7 offset:35632
	ds_write_b16 v192, v8 offset:35904
	ds_write_b16_d16_hi v192, v8 offset:36176
	ds_write_b16 v192, v9 offset:36448
	ds_write_b16_d16_hi v192, v9 offset:36720
	ds_write_b128 v67, v[10:13]
	ds_write_b16 v193, v14 offset:34816
	ds_write_b16_d16_hi v193, v14 offset:35088
	ds_write_b16 v193, v15 offset:35360
	ds_write_b16_d16_hi v193, v15 offset:35632
	ds_write_b16 v193, v16 offset:35904
	ds_write_b16_d16_hi v193, v16 offset:36176
	ds_write_b16 v193, v17 offset:36448
	ds_write_b16_d16_hi v193, v17 offset:36720
	ds_write_b128 v66, v[18:21] offset:17408
	ds_write_b16 v194, v22 offset:34816
	ds_write_b16_d16_hi v194, v22 offset:35088
	ds_write_b16 v194, v23 offset:35360
	ds_write_b16_d16_hi v194, v23 offset:35632
	ds_write_b16 v194, v24 offset:35904
	ds_write_b16_d16_hi v194, v24 offset:36176
	ds_write_b16 v194, v25 offset:36448
	ds_write_b16_d16_hi v194, v25 offset:36720
	v_add_u32_e32 v66, v1, v154
	v_ashrrev_i32_e32 v147, 31, v146
	ds_write_b128 v66, v[26:29]
	ds_write_b16 v195, v30 offset:34816
	ds_write_b16_d16_hi v195, v30 offset:35088
	ds_write_b16 v195, v31 offset:35360
	ds_write_b16_d16_hi v195, v31 offset:35632
	ds_write_b16 v195, v32 offset:35904
	ds_write_b16_d16_hi v195, v32 offset:36176
	ds_write_b16 v195, v33 offset:36448
	ds_write_b16_d16_hi v195, v33 offset:36720
	v_lshlrev_b64 v[66:67], 11, v[146:147]
	v_lshl_add_u64 v[66:67], s[6:7], 0, v[66:67]
	s_lshl_b32 s0, s88, 8
	v_lshl_add_u64 v[66:67], v[66:67], 0, s[0:1]
	v_lshl_add_u64 v[66:67], v[66:67], 0, v[98:99]
	s_waitcnt lgkmcnt(0)
	s_barrier
	global_load_dwordx2 v[144:145], v[66:67], off
	global_load_dwordx2 v[142:143], v[66:67], off offset:32
	global_load_dwordx2 v[140:141], v[66:67], off offset:64
	global_load_dwordx2 v[138:139], v[66:67], off offset:96
	global_load_dwordx2 v[136:137], v[66:67], off offset:128
	global_load_dwordx2 v[134:135], v[66:67], off offset:160
	global_load_dwordx2 v[132:133], v[66:67], off offset:192
	global_load_dwordx2 v[130:131], v[66:67], off offset:224
	s_ashr_i32 s3, s2, 31
	s_lshl_b64 s[92:93], s[2:3], 15
	v_lshl_add_u64 v[74:75], v[100:101], 0, s[92:93]
	v_mov_b32_e32 v103, v99
	v_mov_b32_e32 v105, v99
	v_lshl_add_u64 v[76:77], v[74:75], 0, v[102:103]
	v_lshl_add_u64 v[66:67], v[74:75], 0, v[104:105]
	global_load_dwordx4 v[70:73], v[76:77], off
	s_nop 0
	global_load_dwordx4 v[66:69], v[66:67], off
	v_add_co_u32_e32 v76, vcc, 0x4000, v76
	v_mov_b32_e32 v107, v99
	s_nop 0
	v_addc_co_u32_e32 v77, vcc, 0, v77, vcc
	v_lshl_add_u64 v[74:75], v[74:75], 0, v[106:107]
	global_load_dwordx4 v[78:81], v[76:77], off
	s_nop 0
	global_load_dwordx4 v[74:77], v[74:75], off
	v_readlane_b32 s38, v252, 45
	s_add_i32 s2, s2, s38
	s_cmpk_gt_i32 s2, 0x3ff
	s_cselect_b64 s[92:93], -1, 0
	s_and_b64 vcc, exec, s[92:93]
	v_readlane_b32 s39, v252, 46
	s_cbranch_vccz .Lret_pf_1
	s_waitcnt vmcnt(0)
	s_branch .LBB0_572
.Lret_pf_1:
	s_lshl_b32 s0, s2, 4
	s_and_b32 vcc_lo, s0, 0xffffff80
	s_ashr_i32 vcc_hi, vcc_lo, 31
	s_lshl_b64 s[38:39], vcc, 11
	v_readlane_b32 s0, v252, 47
	s_add_u32 s3, s0, s38
	v_readlane_b32 s0, v252, 49
	s_addc_u32 s37, s0, s39
	s_lshl_b32 s0, s2, 8
	s_and_b32 s0, s0, 0x700
	s_add_u32 s40, s3, s0
	s_addc_u32 s41, s37, 0
	v_readlane_b32 s3, v252, 51
	s_add_u32 s3, s3, s38
	v_readlane_b32 s37, v252, 29
	v_or_b32_e32 v34, vcc_lo, v148
	s_addc_u32 s37, s37, s39
	v_ashrrev_i32_e32 v35, 31, v34
	s_add_u32 s38, s3, s0
	v_lshlrev_b64 v[34:35], 11, v[34:35]
	s_addc_u32 s39, s37, 0
	v_mov_b32_e32 v109, v99
	v_mov_b32_e32 v111, v99
	v_lshl_add_u64 v[34:35], s[4:5], 0, v[34:35]
	v_lshl_add_u64 v[26:27], s[40:41], 0, v[108:109]
	v_lshl_add_u64 v[28:29], s[38:39], 0, v[110:111]
	v_mov_b32_e32 v113, v99
	v_mov_b32_e32 v115, v99
	v_mov_b32_e32 v117, v99
	v_mov_b32_e32 v119, v99
	v_mov_b32_e32 v121, v99
	v_mov_b32_e32 v123, v99
	v_mov_b32_e32 v125, v99
	v_mov_b32_e32 v127, v99
	v_lshl_add_u64 v[34:35], v[34:35], 0, s[0:1]
	v_mov_b32_e32 v129, v99
	v_lshl_add_u64 v[2:3], v[26:27], 0, v[112:113]
	v_lshl_add_u64 v[6:7], v[28:29], 0, v[114:115]
	v_lshl_add_u64 v[10:11], v[26:27], 0, v[116:117]
	v_lshl_add_u64 v[14:15], v[28:29], 0, v[118:119]
	v_lshl_add_u64 v[18:19], v[26:27], 0, v[120:121]
	v_lshl_add_u64 v[22:23], v[28:29], 0, v[122:123]
	v_lshl_add_u64 v[26:27], v[26:27], 0, v[124:125]
	v_lshl_add_u64 v[30:31], v[28:29], 0, v[126:127]
	v_lshl_add_u64 v[46:47], v[34:35], 0, v[128:129]
	global_load_dwordx4 v[2:5], v[2:3], off
	s_nop 0
	global_load_dwordx4 v[6:9], v[6:7], off
	s_nop 0
	global_load_dwordx4 v[10:13], v[10:11], off
	s_nop 0
	global_load_dwordx4 v[14:17], v[14:15], off
	s_nop 0
	global_load_dwordx4 v[18:21], v[18:19], off
	s_nop 0
	global_load_dwordx4 v[22:25], v[22:23], off
	s_nop 0
	global_load_dwordx4 v[26:29], v[26:27], off
	s_nop 0
	global_load_dwordx4 v[30:33], v[30:31], off
	s_nop 0
	global_load_dwordx4 v[34:37], v[46:47], off
	global_load_dwordx4 v[38:41], v[46:47], off offset:64
	global_load_dwordx4 v[42:45], v[46:47], off offset:128
	s_nop 0
	global_load_dwordx4 v[46:49], v[46:47], off offset:192

.LBB0_626:
	s_and_saveexec_b64 vcc, s[74:75]
	ds_write_b32 v156, v82 offset:228
	s_or_b64 exec, exec, vcc
	v_add_u32_e32 v82, v149, v152
	s_waitcnt vmcnt(15)
	ds_write_b128 v82, v[70:73]
	v_add_u32_e32 v70, v149, v153
	s_waitcnt vmcnt(14)
	ds_write_b128 v70, v[66:69]
	s_waitcnt vmcnt(13)
	ds_write_b128 v82, v[78:81] offset:17408
	v_add_u32_e32 v66, v149, v154
	s_waitcnt vmcnt(12)
	ds_write_b128 v66, v[74:77]
	v_mov_b32_e32 v66, 0
	s_lshl_b32 s0, s88, 7
	v_mov_b32_e32 v105, v191
	v_mov_b32_e32 v107, v190
	s_mov_b32 s3, s33
	v_mov_b32_e32 v67, v66
	v_mov_b32_e32 v68, v66
	v_mov_b32_e32 v69, v66
	v_mov_b32_e32 v70, v66
	v_mov_b32_e32 v71, v66
	v_mov_b32_e32 v72, v66
	v_mov_b32_e32 v73, v66
	v_mov_b32_e32 v74, v66
	v_mov_b32_e32 v75, v66
	v_mov_b32_e32 v76, v66
	v_mov_b32_e32 v77, v66
	v_mov_b32_e32 v78, v66
	v_mov_b32_e32 v79, v66
	v_mov_b32_e32 v80, v66
	v_mov_b32_e32 v81, v66
	v_mov_b32_e32 v82, v66
	v_mov_b32_e32 v83, v66
	v_mov_b32_e32 v84, v66
	v_mov_b32_e32 v85, v66
	v_mov_b32_e32 v86, v66
	v_mov_b32_e32 v87, v66
	v_mov_b32_e32 v88, v66
	v_mov_b32_e32 v89, v66
	v_mov_b32_e32 v90, v66
	v_mov_b32_e32 v91, v66
	v_mov_b32_e32 v92, v66
	v_mov_b32_e32 v93, v66
	v_mov_b32_e32 v94, v66
	v_mov_b32_e32 v95, v66
	v_mov_b32_e32 v96, v66
	v_mov_b32_e32 v97, v66
	s_waitcnt lgkmcnt(0)
	s_barrier
.LBB0_629:
	ds_read_b128 v[206:209], v105
	ds_read_b128 v[210:213], v107
	s_waitcnt lgkmcnt(0)
	v_mfma_f32_16x16x32_bf16 v[94:97], v[210:213], v[206:209], v[94:97]
	ds_read_b128 v[210:213], v107 offset:4352
	s_waitcnt lgkmcnt(0)
	v_mfma_f32_16x16x32_bf16 v[90:93], v[210:213], v[206:209], v[90:93]
	ds_read_b128 v[210:213], v107 offset:8704
	s_waitcnt lgkmcnt(0)
	v_mfma_f32_16x16x32_bf16 v[86:89], v[210:213], v[206:209], v[86:89]
	ds_read_b128 v[210:213], v107 offset:13056
	s_waitcnt lgkmcnt(0)
	v_mfma_f32_16x16x32_bf16 v[82:85], v[210:213], v[206:209], v[82:85]
	ds_read_b128 v[210:213], v107 offset:17408
	s_waitcnt lgkmcnt(0)
	v_mfma_f32_16x16x32_bf16 v[78:81], v[210:213], v[206:209], v[78:81]
	ds_read_b128 v[210:213], v107 offset:21760
	s_waitcnt lgkmcnt(0)
	v_mfma_f32_16x16x32_bf16 v[74:77], v[210:213], v[206:209], v[74:77]
	ds_read_b128 v[210:213], v107 offset:26112
	s_waitcnt lgkmcnt(0)
	v_mfma_f32_16x16x32_bf16 v[70:73], v[210:213], v[206:209], v[70:73]
	ds_read_b128 v[210:213], v107 offset:30464
	s_waitcnt lgkmcnt(0)
	v_mfma_f32_16x16x32_bf16 v[66:69], v[210:213], v[206:209], v[66:69]
	s_add_i32 s3, s3, -1
	v_add_u32_e32 v107, 64, v107
	s_cmp_lg_u32 s3, 0
	v_add_u32_e32 v105, 64, v105
	s_cbranch_scc1 .LBB0_629
	ds_read_b128 v[206:209], v196
	ds_read_b128 v[210:213], v196 offset:4352
	ds_read_b128 v[214:217], v196 offset:8704
	ds_read_b128 v[218:221], v196 offset:13056
	ds_read_b128 v[222:225], v196 offset:17408
	ds_read_b128 v[226:229], v196 offset:21760
	ds_read_b128 v[230:233], v196 offset:26112
	ds_read_b128 v[234:237], v196 offset:30464
	s_waitcnt lgkmcnt(7)
	v_mfma_f32_16x16x32_bf16 v[206:209], v[206:209], v[62:65], 0
	s_waitcnt lgkmcnt(6)
	v_mfma_f32_16x16x32_bf16 v[210:213], v[210:213], v[62:65], 0
	s_waitcnt lgkmcnt(5)
	v_mfma_f32_16x16x32_bf16 v[214:217], v[214:217], v[62:65], 0
	s_waitcnt lgkmcnt(4)
	v_mfma_f32_16x16x32_bf16 v[218:221], v[218:221], v[62:65], 0
	s_waitcnt lgkmcnt(3)
	v_mfma_f32_16x16x32_bf16 v[222:225], v[222:225], v[62:65], 0
	s_waitcnt lgkmcnt(2)
	v_mfma_f32_16x16x32_bf16 v[226:229], v[226:229], v[62:65], 0
	s_waitcnt lgkmcnt(1)
	v_mfma_f32_16x16x32_bf16 v[230:233], v[230:233], v[62:65], 0
	s_waitcnt lgkmcnt(0)
	v_mfma_f32_16x16x32_bf16 v[62:65], v[234:237], v[62:65], 0
	ds_read_b128 v[234:237], v196 offset:64
	s_waitcnt lgkmcnt(0)
	v_mfma_f32_16x16x32_bf16 v[206:209], v[234:237], v[58:61], v[206:209]
	ds_read_b128 v[234:237], v196 offset:4416
	s_waitcnt lgkmcnt(0)
	v_mfma_f32_16x16x32_bf16 v[210:213], v[234:237], v[58:61], v[210:213]
	ds_read_b128 v[234:237], v196 offset:8768
	s_waitcnt lgkmcnt(0)
	v_mfma_f32_16x16x32_bf16 v[214:217], v[234:237], v[58:61], v[214:217]
	ds_read_b128 v[234:237], v196 offset:13120
	s_waitcnt lgkmcnt(0)
	v_mfma_f32_16x16x32_bf16 v[218:221], v[234:237], v[58:61], v[218:221]
	ds_read_b128 v[234:237], v196 offset:17472
	s_waitcnt lgkmcnt(0)
	v_mfma_f32_16x16x32_bf16 v[222:225], v[234:237], v[58:61], v[222:225]
	ds_read_b128 v[234:237], v196 offset:21824
	s_waitcnt lgkmcnt(0)
	v_mfma_f32_16x16x32_bf16 v[226:229], v[234:237], v[58:61], v[226:229]
	ds_read_b128 v[234:237], v196 offset:26176
	s_waitcnt lgkmcnt(0)
	v_mfma_f32_16x16x32_bf16 v[230:233], v[234:237], v[58:61], v[230:233]
	ds_read_b128 v[234:237], v196 offset:30528
	s_waitcnt lgkmcnt(0)
	v_mfma_f32_16x16x32_bf16 v[58:61], v[234:237], v[58:61], v[62:65]
	s_nop 2
	ds_read_b128 v[62:65], v196 offset:128
	s_waitcnt lgkmcnt(0)
	v_mfma_f32_16x16x32_bf16 v[62:65], v[62:65], v[54:57], v[206:209]
	s_nop 2
	ds_read_b128 v[206:209], v196 offset:4480
	s_waitcnt lgkmcnt(0)
	v_mfma_f32_16x16x32_bf16 v[206:209], v[206:209], v[54:57], v[210:213]
	s_nop 2
	ds_read_b128 v[210:213], v196 offset:8832
	s_waitcnt lgkmcnt(0)
	v_mfma_f32_16x16x32_bf16 v[210:213], v[210:213], v[54:57], v[214:217]
	s_nop 2
	ds_read_b128 v[214:217], v196 offset:13184
	s_waitcnt lgkmcnt(0)
	v_mfma_f32_16x16x32_bf16 v[214:217], v[214:217], v[54:57], v[218:221]
	s_nop 2
	ds_read_b128 v[218:221], v196 offset:17536
	s_waitcnt lgkmcnt(0)
	v_mfma_f32_16x16x32_bf16 v[218:221], v[218:221], v[54:57], v[222:225]
	s_nop 2
	ds_read_b128 v[222:225], v196 offset:21888
	s_waitcnt lgkmcnt(0)
	v_mfma_f32_16x16x32_bf16 v[222:225], v[222:225], v[54:57], v[226:229]
	s_nop 2
	ds_read_b128 v[226:229], v196 offset:26240
	s_waitcnt lgkmcnt(0)
	v_mfma_f32_16x16x32_bf16 v[226:229], v[226:229], v[54:57], v[230:233]
	s_nop 2
	ds_read_b128 v[230:233], v196 offset:30592
	s_waitcnt lgkmcnt(0)
	v_mfma_f32_16x16x32_bf16 v[54:57], v[230:233], v[54:57], v[58:61]
	s_nop 2
	ds_read_b128 v[58:61], v196 offset:192
	s_waitcnt lgkmcnt(0)
	v_mfma_f32_16x16x32_bf16 v[58:61], v[58:61], v[50:53], v[62:65]
	s_nop 2
	ds_read_b128 v[62:65], v196 offset:4544
	s_waitcnt lgkmcnt(0)
	v_mfma_f32_16x16x32_bf16 v[62:65], v[62:65], v[50:53], v[206:209]
	s_nop 2
	ds_read_b128 v[206:209], v196 offset:8896
	s_waitcnt lgkmcnt(0)
	v_mfma_f32_16x16x32_bf16 v[206:209], v[206:209], v[50:53], v[210:213]
	s_nop 2
	ds_read_b128 v[210:213], v196 offset:13248
	s_waitcnt lgkmcnt(0)
	v_mfma_f32_16x16x32_bf16 v[210:213], v[210:213], v[50:53], v[214:217]
	s_nop 2
	ds_read_b128 v[214:217], v196 offset:17600
	s_waitcnt lgkmcnt(0)
	v_mfma_f32_16x16x32_bf16 v[214:217], v[214:217], v[50:53], v[218:221]
	s_nop 2
	ds_read_b128 v[218:221], v196 offset:21952
	s_waitcnt lgkmcnt(0)
	v_mfma_f32_16x16x32_bf16 v[218:221], v[218:221], v[50:53], v[222:225]
	s_nop 2
	ds_read_b128 v[222:225], v196 offset:26304
	s_waitcnt lgkmcnt(0)
	v_mfma_f32_16x16x32_bf16 v[222:225], v[222:225], v[50:53], v[226:229]
	s_nop 2
	ds_read_b128 v[226:229], v196 offset:30656
	s_waitcnt lgkmcnt(0)
	v_mfma_f32_16x16x32_bf16 v[226:229], v[226:229], v[50:53], v[54:57]
	v_mul_f32_e32 v50, v103, v157
	v_cmp_gt_f32_e32 vcc, s89, v50
	s_mov_b32 s3, 0xf800000
	s_lshl_b32 s0, s0, 1
	v_cndmask_b32_e32 v51, 0, v200, vcc
	v_fmac_f32_e32 v51, v103, v157
	v_exp_f32_e32 v51, v51
	v_cndmask_b32_e32 v50, 0, v203, vcc
	v_ldexp_f32 v52, v51, v50
	v_pk_fma_f32 v[94:95], v[52:53], v[58:59], v[94:95] op_sel_hi:[0,1,1]
	v_pk_fma_f32 v[90:91], v[52:53], v[62:63], v[90:91] op_sel_hi:[0,1,1]
	v_pk_fma_f32 v[96:97], v[52:53], v[60:61], v[96:97] op_sel_hi:[0,1,1]
	v_pk_fma_f32 v[92:93], v[52:53], v[64:65], v[92:93] op_sel_hi:[0,1,1]
	v_mov_b32_e32 v50, v94
	v_mov_b32_e32 v51, v90
	v_mov_b32_e32 v54, v95
	v_mov_b32_e32 v55, v91
	v_pk_add_f32 v[50:51], v[50:51], v[54:55]
	v_mov_b32_e32 v54, v96
	v_mov_b32_e32 v55, v92
	v_mov_b32_e32 v56, v97
	v_mov_b32_e32 v57, v93
	v_pk_add_f32 v[54:55], v[54:55], v[56:57]
	v_pk_fma_f32 v[86:87], v[52:53], v[206:207], v[86:87] op_sel_hi:[0,1,1]
	v_pk_fma_f32 v[88:89], v[52:53], v[208:209], v[88:89] op_sel_hi:[0,1,1]
	v_pk_add_f32 v[50:51], v[50:51], v[54:55]
	v_pk_mov_b32 v[54:55], v[86:87], v[88:89] op_sel:[1,0]
	v_mov_b32_e32 v56, v86
	v_mov_b32_e32 v57, v89
	v_pk_add_f32 v[54:55], v[54:55], v[56:57]
	v_add_f32_e32 v50, 0, v50
	v_pk_add_f32 v[54:55], v[54:55], v[54:55] op_sel:[0,1] op_sel_hi:[1,0]
	v_pk_fma_f32 v[84:85], v[52:53], v[212:213], v[84:85] op_sel_hi:[0,1,1]
	v_pk_fma_f32 v[82:83], v[52:53], v[210:211], v[82:83] op_sel_hi:[0,1,1]
	v_pk_fma_f32 v[62:63], v[52:53], v[216:217], v[80:81] op_sel_hi:[0,1,1]
	v_pk_fma_f32 v[64:65], v[52:53], v[214:215], v[78:79] op_sel_hi:[0,1,1]
	v_add_f32_e32 v50, v50, v51
	v_add_f32_e32 v56, v82, v83
	v_add_f32_e32 v58, v84, v85
	v_mov_b32_e32 v51, v64
	v_mov_b32_e32 v55, v65
	v_mov_b32_e32 v57, v62
	v_mov_b32_e32 v59, v63
	v_pk_add_f32 v[50:51], v[50:51], v[54:55]
	v_pk_add_f32 v[54:55], v[56:57], v[58:59]
	v_pk_fma_f32 v[58:59], v[52:53], v[218:219], v[74:75] op_sel_hi:[0,1,1]
	v_pk_add_f32 v[50:51], v[50:51], v[54:55]
	v_pk_fma_f32 v[60:61], v[52:53], v[220:221], v[76:77] op_sel_hi:[0,1,1]
	v_pk_add_f32 v[78:79], v[50:51], v[50:51] op_sel:[0,1] op_sel_hi:[1,0]
	v_pk_mov_b32 v[50:51], v[58:59], v[60:61] op_sel:[1,0]
	v_mov_b32_e32 v54, v58
	v_mov_b32_e32 v55, v61
	v_pk_add_f32 v[50:51], v[50:51], v[54:55]
	v_pk_fma_f32 v[54:55], v[52:53], v[224:225], v[72:73] op_sel_hi:[0,1,1]
	v_pk_add_f32 v[74:75], v[50:51], v[50:51] op_sel:[0,1] op_sel_hi:[1,0]
	v_pk_fma_f32 v[56:57], v[52:53], v[222:223], v[70:71] op_sel_hi:[0,1,1]
	v_pk_fma_f32 v[50:51], v[52:53], v[228:229], v[68:69] op_sel_hi:[0,1,1]
	v_pk_fma_f32 v[52:53], v[52:53], v[226:227], v[66:67] op_sel_hi:[0,1,1]
	v_add_f32_e32 v70, v56, v57
	v_add_f32_e32 v72, v54, v55
	v_mov_b32_e32 v79, v52
	v_mov_b32_e32 v75, v53
	v_mov_b32_e32 v71, v50
	v_mov_b32_e32 v73, v51
	v_pk_add_f32 v[66:67], v[78:79], v[74:75]
	v_pk_add_f32 v[68:69], v[70:71], v[72:73]
	s_nop 0
	v_pk_add_f32 v[66:67], v[66:67], v[68:69]
	s_nop 0
	v_add_f32_e32 v66, v66, v67
	ds_bpermute_b32 v67, v150, v66
	s_waitcnt lgkmcnt(0)
	v_add_f32_e32 v66, v66, v67
	ds_bpermute_b32 v67, v151, v66
	s_waitcnt lgkmcnt(0)
	v_add_f32_e32 v103, v66, v67
	v_fmamk_f32 v70, v103, 0xbc000000, v97
	v_fmamk_f32 v72, v103, 0xbc000000, v95
	v_fmamk_f32 v71, v103, 0xbc000000, v93
	v_fmac_f32_e32 v92, 0xbc000000, v103
	v_fmamk_f32 v73, v103, 0xbc000000, v91
	v_fmac_f32_e32 v90, 0xbc000000, v103
	v_fmac_f32_e32 v96, 0xbc000000, v103
	v_fmac_f32_e32 v94, 0xbc000000, v103
	v_mov_b32_e32 v95, v90
	v_pk_mul_f32 v[66:67], v[72:73], v[72:73]
	v_mov_b32_e32 v97, v92
	v_pk_mul_f32 v[68:69], v[70:71], v[70:71]
	v_pk_fma_f32 v[66:67], v[94:95], v[94:95], v[66:67]
	v_pk_fma_f32 v[68:69], v[96:97], v[96:97], v[68:69]
	v_fmamk_f32 v87, v103, 0xbc000000, v87
	v_pk_add_f32 v[66:67], v[66:67], v[68:69]
	v_fmac_f32_e32 v86, 0xbc000000, v103
	v_fmamk_f32 v89, v103, 0xbc000000, v89
	v_fmac_f32_e32 v88, 0xbc000000, v103
	v_pk_add_f32 v[66:67], v[66:67], v[66:67] op_sel_hi:[0,1]
	v_pk_mul_f32 v[68:69], v[88:89], v[88:89]
	v_pk_mul_f32 v[74:75], v[86:87], v[86:87]
	v_fmac_f32_e32 v82, 0xbc000000, v103
	v_pk_mov_b32 v[76:77], v[74:75], v[68:69] op_sel:[1,0]
	v_mov_b32_e32 v75, v69
	v_fmamk_f32 v83, v103, 0xbc000000, v83
	v_fmac_f32_e32 v84, 0xbc000000, v103
	v_mul_f32_e32 v66, v82, v82
	v_pk_add_f32 v[68:69], v[76:77], v[74:75]
	v_fmamk_f32 v85, v103, 0xbc000000, v85
	v_pk_fma_f32 v[76:77], v[82:83], v[82:83], v[66:67] op_sel_hi:[1,1,0]
	v_mul_f32_e32 v66, v84, v84
	v_pk_add_f32 v[74:75], v[68:69], v[68:69] op_sel_hi:[0,1]
	v_pk_fma_f32 v[78:79], v[84:85], v[84:85], v[66:67] op_sel_hi:[1,1,0]
	v_fmamk_f32 v69, v103, 0xbc000000, v63
	v_fmac_f32_e32 v62, 0xbc000000, v103
	v_fmamk_f32 v68, v103, 0xbc000000, v65
	v_fmac_f32_e32 v64, 0xbc000000, v103
	v_mul_f32_e32 v76, v64, v64
	v_mul_f32_e32 v78, v68, v68
	v_mul_f32_e32 v74, v62, v62
	v_mul_f32_e32 v66, v69, v69
	v_pk_add_f32 v[76:77], v[76:77], v[78:79]
	v_pk_add_f32 v[66:67], v[74:75], v[66:67]
	v_fmamk_f32 v59, v103, 0xbc000000, v59
	v_pk_add_f32 v[66:67], v[76:77], v[66:67]
	v_fmac_f32_e32 v58, 0xbc000000, v103
	v_fmamk_f32 v61, v103, 0xbc000000, v61
	v_fmac_f32_e32 v60, 0xbc000000, v103
	v_pk_add_f32 v[74:75], v[66:67], v[66:67] op_sel_hi:[0,1]
	v_pk_mul_f32 v[66:67], v[60:61], v[60:61]
	v_pk_mul_f32 v[76:77], v[58:59], v[58:59]
	v_fmac_f32_e32 v56, 0xbc000000, v103
	v_pk_mov_b32 v[78:79], v[76:77], v[66:67] op_sel:[1,0]
	v_mov_b32_e32 v77, v67
	v_pk_add_f32 v[66:67], v[78:79], v[76:77]
	v_fmamk_f32 v57, v103, 0xbc000000, v57
	v_pk_add_f32 v[76:77], v[66:67], v[66:67] op_sel_hi:[0,1]
	v_fmac_f32_e32 v54, 0xbc000000, v103
	v_mul_f32_e32 v66, v56, v56
	v_fmamk_f32 v55, v103, 0xbc000000, v55
	v_pk_fma_f32 v[78:79], v[56:57], v[56:57], v[66:67] op_sel_hi:[1,1,0]
	v_mul_f32_e32 v66, v54, v54
	v_pk_fma_f32 v[80:81], v[54:55], v[54:55], v[66:67] op_sel_hi:[1,1,0]
	v_fmamk_f32 v67, v103, 0xbc000000, v51
	v_fmac_f32_e32 v50, 0xbc000000, v103
	v_fmamk_f32 v66, v103, 0xbc000000, v53
	v_fmac_f32_e32 v52, 0xbc000000, v103
	v_mul_f32_e32 v78, v52, v52
	v_mul_f32_e32 v80, v66, v66
	v_mul_f32_e32 v76, v50, v50
	v_mul_f32_e32 v74, v67, v67
	v_pk_add_f32 v[78:79], v[78:79], v[80:81]
	v_pk_add_f32 v[74:75], v[76:77], v[74:75]
	v_mov_b32_e32 v95, v96
	v_pk_add_f32 v[74:75], v[78:79], v[74:75]
	v_lshlrev_b32_e32 v81, 16, v145
	v_add_f32_e32 v51, v74, v75
	ds_bpermute_b32 v53, v150, v51
	v_lshlrev_b32_e32 v80, 16, v144
	v_lshlrev_b64 v[76:77], 12, v[146:147]
	v_lshl_add_u64 v[76:77], s[90:91], 0, v[76:77]
	v_lshl_add_u64 v[76:77], v[76:77], 0, s[0:1]
	s_waitcnt lgkmcnt(0)
	v_add_f32_e32 v51, v51, v53
	ds_bpermute_b32 v53, v151, v51
	v_lshl_add_u64 v[76:77], v[76:77], 0, v[98:99]
	v_mov_b32_e32 v91, v92
	s_waitcnt lgkmcnt(0)
	v_add_f32_e32 v51, v51, v53
	v_fmamk_f32 v51, v51, 0x3c000000, v197
	v_mul_f32_e32 v53, 0x4f800000, v51
	v_cmp_gt_f32_e32 vcc, s3, v51
	s_nop 1
	v_cndmask_b32_e32 v51, v51, v53, vcc
	v_sqrt_f32_e32 v53, v51
	s_nop 0
	v_add_u32_e32 v63, -1, v53
	v_fma_f32 v65, -v63, v53, v51
	v_cmp_ge_f32_e64 s[74:75], 0, v65
	v_add_u32_e32 v65, 1, v53
	s_nop 0
	v_cndmask_b32_e64 v63, v53, v63, s[74:75]
	v_fma_f32 v53, -v65, v53, v51
	v_cmp_lt_f32_e64 s[74:75], 0, v53
	s_nop 1
	v_cndmask_b32_e64 v53, v63, v65, s[74:75]
	v_mul_f32_e32 v63, 0x37800000, v53
	v_cndmask_b32_e32 v53, v53, v63, vcc
	v_cmp_class_f32_e32 vcc, v51, v199
	s_nop 1
	v_cndmask_b32_e32 v51, v53, v51, vcc
	v_div_scale_f32 v53, s[36:37], v51, v51, 1.0
	v_rcp_f32_e32 v63, v53
	s_nop 0
	v_fma_f32 v65, -v53, v63, 1.0
	v_fmac_f32_e32 v63, v65, v63
	v_div_scale_f32 v65, vcc, 1.0, v51, 1.0
	v_mul_f32_e32 v74, v65, v63
	v_fma_f32 v75, -v53, v74, v65
	v_fmac_f32_e32 v74, v75, v63
	v_fma_f32 v53, -v53, v74, v65
	v_div_fmas_f32 v53, v53, v63, v74
	v_div_fixup_f32 v74, v53, v51, 1.0
	v_pk_mul_f32 v[78:79], v[94:95], v[74:75] op_sel_hi:[1,0]
	v_and_b32_e32 v95, 0xffff0000, v145
	v_pk_mul_f32 v[78:79], v[78:79], v[80:81]
	v_mov_b32_e32 v80, v72
	v_mov_b32_e32 v81, v70
	v_pk_mul_f32 v[80:81], v[80:81], v[74:75] op_sel_hi:[1,0]
	v_and_b32_e32 v94, 0xffff0000, v144
	v_pk_mul_f32 v[80:81], v[80:81], v[94:95]
	v_and_b32_sdwa v51, v79, v204 dst_sel:DWORD dst_unused:UNUSED_PAD src0_sel:WORD_1 src1_sel:DWORD
	v_and_b32_sdwa v63, v81, v204 dst_sel:DWORD dst_unused:UNUSED_PAD src0_sel:WORD_1 src1_sel:DWORD
	v_and_b32_sdwa v65, v80, v204 dst_sel:DWORD dst_unused:UNUSED_PAD src0_sel:WORD_1 src1_sel:DWORD
	v_and_b32_sdwa v53, v78, v204 dst_sel:DWORD dst_unused:UNUSED_PAD src0_sel:WORD_1 src1_sel:DWORD
	v_add3_u32 v63, v81, v63, s34
	v_add3_u32 v65, v80, v65, s34
	v_add3_u32 v53, v78, v53, s34
	v_add3_u32 v51, v79, v51, s34
	v_and_b32_e32 v63, 0xffff0000, v63
	v_and_b32_e32 v65, 0xffff0000, v65
	v_mov_b32_e32 v70, v73
	v_or_b32_sdwa v79, v63, v51 dst_sel:DWORD dst_unused:UNUSED_PAD src0_sel:DWORD src1_sel:WORD_1
	v_or_b32_sdwa v78, v65, v53 dst_sel:DWORD dst_unused:UNUSED_PAD src0_sel:DWORD src1_sel:WORD_1
	v_pk_mul_f32 v[70:71], v[70:71], v[74:75] op_sel_hi:[1,0]
	v_and_b32_e32 v73, 0xffff0000, v143
	v_and_b32_e32 v72, 0xffff0000, v142
	global_store_dwordx2 v[76:77], v[78:79], off offset:2048
	v_pk_mul_f32 v[78:79], v[90:91], v[74:75] op_sel_hi:[1,0]
	v_lshlrev_b32_e32 v81, 16, v143
	v_lshlrev_b32_e32 v80, 16, v142
	v_pk_mul_f32 v[70:71], v[70:71], v[72:73]
	v_pk_mul_f32 v[78:79], v[78:79], v[80:81]
	v_and_b32_sdwa v63, v71, v204 dst_sel:DWORD dst_unused:UNUSED_PAD src0_sel:WORD_1 src1_sel:DWORD
	v_and_b32_sdwa v65, v70, v204 dst_sel:DWORD dst_unused:UNUSED_PAD src0_sel:WORD_1 src1_sel:DWORD
	v_and_b32_sdwa v51, v79, v204 dst_sel:DWORD dst_unused:UNUSED_PAD src0_sel:WORD_1 src1_sel:DWORD
	v_and_b32_sdwa v53, v78, v204 dst_sel:DWORD dst_unused:UNUSED_PAD src0_sel:WORD_1 src1_sel:DWORD
	v_add3_u32 v63, v71, v63, s34
	v_add3_u32 v65, v70, v65, s34
	v_add3_u32 v53, v78, v53, s34
	v_add3_u32 v51, v79, v51, s34
	v_and_b32_e32 v63, 0xffff0000, v63
	v_and_b32_e32 v65, 0xffff0000, v65
	v_or_b32_sdwa v71, v63, v51 dst_sel:DWORD dst_unused:UNUSED_PAD src0_sel:DWORD src1_sel:WORD_1
	v_or_b32_sdwa v70, v65, v53 dst_sel:DWORD dst_unused:UNUSED_PAD src0_sel:DWORD src1_sel:WORD_1
	global_store_dwordx2 v[76:77], v[70:71], off offset:2080
	v_mov_b32_e32 v70, v86
	v_mov_b32_e32 v71, v88
	v_pk_mul_f32 v[70:71], v[70:71], v[74:75] op_sel_hi:[1,0]
	v_lshlrev_b32_e32 v73, 16, v141
	v_lshlrev_b32_e32 v72, 16, v140
	v_mov_b32_e32 v88, v87
	v_pk_mul_f32 v[70:71], v[70:71], v[72:73]
	v_pk_mul_f32 v[72:73], v[88:89], v[74:75] op_sel_hi:[1,0]
	v_and_b32_e32 v79, 0xffff0000, v141
	v_and_b32_e32 v78, 0xffff0000, v140
	v_pk_mul_f32 v[72:73], v[72:73], v[78:79]
	v_and_b32_sdwa v51, v71, v204 dst_sel:DWORD dst_unused:UNUSED_PAD src0_sel:WORD_1 src1_sel:DWORD
	v_and_b32_sdwa v63, v73, v204 dst_sel:DWORD dst_unused:UNUSED_PAD src0_sel:WORD_1 src1_sel:DWORD
	v_and_b32_sdwa v65, v72, v204 dst_sel:DWORD dst_unused:UNUSED_PAD src0_sel:WORD_1 src1_sel:DWORD
	v_and_b32_sdwa v53, v70, v204 dst_sel:DWORD dst_unused:UNUSED_PAD src0_sel:WORD_1 src1_sel:DWORD
	v_add3_u32 v63, v73, v63, s34
	v_add3_u32 v65, v72, v65, s34
	v_add3_u32 v53, v70, v53, s34
	v_add3_u32 v51, v71, v51, s34
	v_and_b32_e32 v63, 0xffff0000, v63
	v_and_b32_e32 v65, 0xffff0000, v65
	v_or_b32_sdwa v71, v63, v51 dst_sel:DWORD dst_unused:UNUSED_PAD src0_sel:DWORD src1_sel:WORD_1
	v_or_b32_sdwa v70, v65, v53 dst_sel:DWORD dst_unused:UNUSED_PAD src0_sel:DWORD src1_sel:WORD_1
	global_store_dwordx2 v[76:77], v[70:71], off offset:2112
	v_mov_b32_e32 v70, v82
	v_mov_b32_e32 v71, v84
	v_pk_mul_f32 v[70:71], v[70:71], v[74:75] op_sel_hi:[1,0]
	v_lshlrev_b32_e32 v73, 16, v139
	v_lshlrev_b32_e32 v72, 16, v138
	v_mov_b32_e32 v84, v83
	v_pk_mul_f32 v[70:71], v[70:71], v[72:73]
	v_pk_mul_f32 v[72:73], v[84:85], v[74:75] op_sel_hi:[1,0]
	v_and_b32_e32 v79, 0xffff0000, v139
	v_and_b32_e32 v78, 0xffff0000, v138
	v_pk_mul_f32 v[72:73], v[72:73], v[78:79]
	v_and_b32_sdwa v53, v70, v204 dst_sel:DWORD dst_unused:UNUSED_PAD src0_sel:WORD_1 src1_sel:DWORD
	v_and_b32_sdwa v65, v72, v204 dst_sel:DWORD dst_unused:UNUSED_PAD src0_sel:WORD_1 src1_sel:DWORD
	v_and_b32_sdwa v63, v73, v204 dst_sel:DWORD dst_unused:UNUSED_PAD src0_sel:WORD_1 src1_sel:DWORD
	v_add3_u32 v65, v72, v65, s34
	v_and_b32_sdwa v51, v71, v204 dst_sel:DWORD dst_unused:UNUSED_PAD src0_sel:WORD_1 src1_sel:DWORD
	v_add3_u32 v53, v70, v53, s34
	v_add3_u32 v63, v73, v63, s34
	v_and_b32_e32 v65, 0xffff0000, v65
	v_add3_u32 v51, v71, v51, s34
	v_and_b32_e32 v63, 0xffff0000, v63
	v_or_b32_sdwa v70, v65, v53 dst_sel:DWORD dst_unused:UNUSED_PAD src0_sel:DWORD src1_sel:WORD_1
	v_mov_b32_e32 v65, v62
	v_or_b32_sdwa v71, v63, v51 dst_sel:DWORD dst_unused:UNUSED_PAD src0_sel:DWORD src1_sel:WORD_1
	v_pk_mul_f32 v[62:63], v[64:65], v[74:75] op_sel_hi:[1,0]
	v_lshlrev_b32_e32 v65, 16, v137
	v_lshlrev_b32_e32 v64, 16, v136
	v_pk_mul_f32 v[62:63], v[62:63], v[64:65]
	v_pk_mul_f32 v[64:65], v[68:69], v[74:75] op_sel_hi:[1,0]
	v_and_b32_e32 v69, 0xffff0000, v137
	v_and_b32_e32 v68, 0xffff0000, v136
	v_pk_mul_f32 v[64:65], v[64:65], v[68:69]
	v_and_b32_sdwa v51, v63, v204 dst_sel:DWORD dst_unused:UNUSED_PAD src0_sel:WORD_1 src1_sel:DWORD
	v_and_b32_sdwa v53, v62, v204 dst_sel:DWORD dst_unused:UNUSED_PAD src0_sel:WORD_1 src1_sel:DWORD
	v_add3_u32 v53, v62, v53, s34
	v_add3_u32 v51, v63, v51, s34
	v_and_b32_sdwa v62, v65, v204 dst_sel:DWORD dst_unused:UNUSED_PAD src0_sel:WORD_1 src1_sel:DWORD
	v_and_b32_sdwa v63, v64, v204 dst_sel:DWORD dst_unused:UNUSED_PAD src0_sel:WORD_1 src1_sel:DWORD
	v_add3_u32 v62, v65, v62, s34
	v_add3_u32 v63, v64, v63, s34
	v_and_b32_e32 v62, 0xffff0000, v62
	v_and_b32_e32 v64, 0xffff0000, v63
	v_or_b32_sdwa v63, v62, v51 dst_sel:DWORD dst_unused:UNUSED_PAD src0_sel:DWORD src1_sel:WORD_1
	v_or_b32_sdwa v62, v64, v53 dst_sel:DWORD dst_unused:UNUSED_PAD src0_sel:DWORD src1_sel:WORD_1
	global_store_dwordx2 v[76:77], v[62:63], off offset:2176
	v_mov_b32_e32 v63, v60
	v_mov_b32_e32 v60, v59
	v_mov_b32_e32 v62, v58
	v_pk_mul_f32 v[58:59], v[60:61], v[74:75] op_sel_hi:[1,0]
	v_and_b32_e32 v61, 0xffff0000, v135
	v_and_b32_e32 v60, 0xffff0000, v134
	v_pk_mul_f32 v[62:63], v[62:63], v[74:75] op_sel_hi:[1,0]
	v_lshlrev_b32_e32 v65, 16, v135
	v_lshlrev_b32_e32 v64, 16, v134
	v_pk_mul_f32 v[58:59], v[58:59], v[60:61]
	v_pk_mul_f32 v[62:63], v[62:63], v[64:65]
	v_and_b32_sdwa v60, v59, v204 dst_sel:DWORD dst_unused:UNUSED_PAD src0_sel:WORD_1 src1_sel:DWORD
	v_and_b32_sdwa v61, v58, v204 dst_sel:DWORD dst_unused:UNUSED_PAD src0_sel:WORD_1 src1_sel:DWORD
	v_and_b32_sdwa v51, v63, v204 dst_sel:DWORD dst_unused:UNUSED_PAD src0_sel:WORD_1 src1_sel:DWORD
	v_and_b32_sdwa v53, v62, v204 dst_sel:DWORD dst_unused:UNUSED_PAD src0_sel:WORD_1 src1_sel:DWORD
	v_add3_u32 v59, v59, v60, s34
	v_add3_u32 v58, v58, v61, s34
	v_add3_u32 v53, v62, v53, s34
	v_add3_u32 v51, v63, v51, s34
	v_and_b32_e32 v59, 0xffff0000, v59
	v_and_b32_e32 v58, 0xffff0000, v58
	v_or_b32_sdwa v59, v59, v51 dst_sel:DWORD dst_unused:UNUSED_PAD src0_sel:DWORD src1_sel:WORD_1
	v_or_b32_sdwa v58, v58, v53 dst_sel:DWORD dst_unused:UNUSED_PAD src0_sel:DWORD src1_sel:WORD_1
	global_store_dwordx2 v[76:77], v[58:59], off offset:2208
	v_mov_b32_e32 v59, v54
	v_mov_b32_e32 v54, v57
	v_mov_b32_e32 v58, v56
	v_pk_mul_f32 v[54:55], v[54:55], v[74:75] op_sel_hi:[1,0]
	v_and_b32_e32 v57, 0xffff0000, v133
	v_and_b32_e32 v56, 0xffff0000, v132
	v_pk_mul_f32 v[58:59], v[58:59], v[74:75] op_sel_hi:[1,0]
	v_lshlrev_b32_e32 v61, 16, v133
	v_lshlrev_b32_e32 v60, 16, v132
	v_pk_mul_f32 v[54:55], v[54:55], v[56:57]
	v_pk_mul_f32 v[58:59], v[58:59], v[60:61]
	v_and_b32_sdwa v57, v54, v204 dst_sel:DWORD dst_unused:UNUSED_PAD src0_sel:WORD_1 src1_sel:DWORD
	v_and_b32_sdwa v53, v58, v204 dst_sel:DWORD dst_unused:UNUSED_PAD src0_sel:WORD_1 src1_sel:DWORD
	v_and_b32_sdwa v56, v55, v204 dst_sel:DWORD dst_unused:UNUSED_PAD src0_sel:WORD_1 src1_sel:DWORD
	v_add3_u32 v54, v54, v57, s34
	v_and_b32_sdwa v51, v59, v204 dst_sel:DWORD dst_unused:UNUSED_PAD src0_sel:WORD_1 src1_sel:DWORD
	v_add3_u32 v53, v58, v53, s34
	v_add3_u32 v55, v55, v56, s34
	v_and_b32_e32 v54, 0xffff0000, v54
	v_add3_u32 v51, v59, v51, s34
	v_and_b32_e32 v55, 0xffff0000, v55
	v_or_b32_sdwa v54, v54, v53 dst_sel:DWORD dst_unused:UNUSED_PAD src0_sel:DWORD src1_sel:WORD_1
	v_mov_b32_e32 v53, v50
	v_or_b32_sdwa v55, v55, v51 dst_sel:DWORD dst_unused:UNUSED_PAD src0_sel:DWORD src1_sel:WORD_1
	v_pk_mul_f32 v[50:51], v[52:53], v[74:75] op_sel_hi:[1,0]
	v_lshlrev_b32_e32 v53, 16, v131
	v_lshlrev_b32_e32 v52, 16, v130
	global_store_dwordx2 v[76:77], v[54:55], off offset:2240
	v_pk_mul_f32 v[50:51], v[50:51], v[52:53]
	v_pk_mul_f32 v[52:53], v[66:67], v[74:75] op_sel_hi:[1,0]
	v_and_b32_e32 v55, 0xffff0000, v131
	v_and_b32_e32 v54, 0xffff0000, v130
	v_pk_mul_f32 v[52:53], v[52:53], v[54:55]
	v_and_b32_sdwa v54, v51, v204 dst_sel:DWORD dst_unused:UNUSED_PAD src0_sel:WORD_1 src1_sel:DWORD
	v_and_b32_sdwa v55, v50, v204 dst_sel:DWORD dst_unused:UNUSED_PAD src0_sel:WORD_1 src1_sel:DWORD
	v_add3_u32 v50, v50, v55, s34
	v_add3_u32 v51, v51, v54, s34
	v_and_b32_sdwa v54, v53, v204 dst_sel:DWORD dst_unused:UNUSED_PAD src0_sel:WORD_1 src1_sel:DWORD
	v_and_b32_sdwa v55, v52, v204 dst_sel:DWORD dst_unused:UNUSED_PAD src0_sel:WORD_1 src1_sel:DWORD
	v_add3_u32 v53, v53, v54, s34
	v_add3_u32 v52, v52, v55, s34
	v_and_b32_e32 v53, 0xffff0000, v53
	v_and_b32_e32 v52, 0xffff0000, v52
	v_or_b32_sdwa v51, v53, v51 dst_sel:DWORD dst_unused:UNUSED_PAD src0_sel:DWORD src1_sel:WORD_1
	v_or_b32_sdwa v50, v52, v50 dst_sel:DWORD dst_unused:UNUSED_PAD src0_sel:DWORD src1_sel:WORD_1
	global_store_dwordx2 v[76:77], v[50:51], off offset:2272
	s_waitcnt vmcnt(7)
	v_mov_b64_e32 v[64:65], v[36:37]
	v_mov_b64_e32 v[60:61], v[40:41]
	v_mov_b64_e32 v[56:57], v[44:45]
	v_mov_b64_e32 v[52:53], v[48:49]
	s_andn2_b64 vcc, exec, s[92:93]
	v_mov_b64_e32 v[62:63], v[34:35]
	v_mov_b64_e32 v[58:59], v[38:39]
	v_mov_b64_e32 v[54:55], v[42:43]
	v_mov_b64_e32 v[50:51], v[46:47]
	global_store_dwordx2 v[76:77], v[70:71], off offset:2144
	s_barrier
	s_cbranch_vccnz .LBB0_570

.LBB0_656:
	s_and_b32 s88, s92, 7
	v_cvt_f32_ubyte0_e32 v66, s88
	v_sub_f32_e32 v82, 0xc0a00000, v66
	s_lshl_b32 s0, s92, 4
	v_cmp_gt_f32_e64 s[74:75], s89, v82
	s_and_b64 s[30:31], s[74:75], exec
	s_cselect_b32 s34, 0xffffffc0, 0
	s_and_b32 s0, s0, 0xffffff80
	v_add_u32_e32 v66, v148, v152
	v_add_u32_e32 v67, v148, v153
	v_add_u32_e32 v146, s0, v155
	ds_write_b128 v66, v[2:5]
	ds_write_b16 v192, v6 offset:34816
	ds_write_b16_d16_hi v192, v6 offset:35088
	ds_write_b16 v192, v7 offset:35360
	ds_write_b16_d16_hi v192, v7 offset:35632
	ds_write_b16 v192, v8 offset:35904
	ds_write_b16_d16_hi v192, v8 offset:36176
	ds_write_b16 v192, v9 offset:36448
	ds_write_b16_d16_hi v192, v9 offset:36720
	ds_write_b128 v67, v[10:13]
	ds_write_b16 v193, v14 offset:34816
	ds_write_b16_d16_hi v193, v14 offset:35088
	ds_write_b16 v193, v15 offset:35360
	ds_write_b16_d16_hi v193, v15 offset:35632
	ds_write_b16 v193, v16 offset:35904
	ds_write_b16_d16_hi v193, v16 offset:36176
	ds_write_b16 v193, v17 offset:36448
	ds_write_b16_d16_hi v193, v17 offset:36720
	ds_write_b128 v66, v[18:21] offset:17408
	ds_write_b16 v195, v22 offset:34816
	ds_write_b16_d16_hi v195, v22 offset:35088
	ds_write_b16 v195, v23 offset:35360
	ds_write_b16_d16_hi v195, v23 offset:35632
	ds_write_b16 v195, v24 offset:35904
	ds_write_b16_d16_hi v195, v24 offset:36176
	ds_write_b16 v195, v25 offset:36448
	ds_write_b16_d16_hi v195, v25 offset:36720
	v_add_u32_e32 v66, v148, v154
	v_ashrrev_i32_e32 v147, 31, v146
	ds_write_b128 v66, v[26:29]
	ds_write_b16 v196, v30 offset:34816
	ds_write_b16_d16_hi v196, v30 offset:35088
	ds_write_b16 v196, v31 offset:35360
	ds_write_b16_d16_hi v196, v31 offset:35632
	ds_write_b16 v196, v32 offset:35904
	ds_write_b16_d16_hi v196, v32 offset:36176
	ds_write_b16 v196, v33 offset:36448
	ds_write_b16_d16_hi v196, v33 offset:36720
	v_lshlrev_b64 v[66:67], 11, v[146:147]
	v_lshl_add_u64 v[66:67], s[6:7], 0, v[66:67]
	s_lshl_b32 s0, s88, 8
	v_lshl_add_u64 v[66:67], v[66:67], 0, s[0:1]
	v_lshl_add_u64 v[66:67], v[66:67], 0, v[98:99]
	s_waitcnt lgkmcnt(0)
	s_barrier
	global_load_dwordx2 v[144:145], v[66:67], off
	global_load_dwordx2 v[142:143], v[66:67], off offset:32
	global_load_dwordx2 v[140:141], v[66:67], off offset:64
	global_load_dwordx2 v[138:139], v[66:67], off offset:96
	global_load_dwordx2 v[136:137], v[66:67], off offset:128
	global_load_dwordx2 v[134:135], v[66:67], off offset:160
	global_load_dwordx2 v[132:133], v[66:67], off offset:192
	global_load_dwordx2 v[130:131], v[66:67], off offset:224
	s_ashr_i32 s93, s92, 31
	s_lshl_b64 s[30:31], s[92:93], 15
	v_lshl_add_u64 v[74:75], v[100:101], 0, s[30:31]
	v_mov_b32_e32 v103, v99
	v_mov_b32_e32 v105, v99
	v_lshl_add_u64 v[76:77], v[74:75], 0, v[102:103]
	v_lshl_add_u64 v[66:67], v[74:75], 0, v[104:105]
	global_load_dwordx4 v[70:73], v[76:77], off
	s_nop 0
	global_load_dwordx4 v[66:69], v[66:67], off
	v_add_co_u32_e32 v76, vcc, 0x4000, v76
	v_mov_b32_e32 v107, v99
	s_nop 0
	v_addc_co_u32_e32 v77, vcc, 0, v77, vcc
	v_lshl_add_u64 v[74:75], v[74:75], 0, v[106:107]
	global_load_dwordx4 v[78:81], v[76:77], off
	s_nop 0
	global_load_dwordx4 v[74:77], v[74:75], off
	v_readlane_b32 s30, v252, 45
	s_add_i32 s92, s92, s30
	v_readlane_b32 s31, v252, 46
	s_cmpk_gt_i32 s92, 0x3ff
	s_cselect_b64 s[30:31], -1, 0
	s_and_b64 vcc, exec, s[30:31]
	s_cbranch_vccz .Lret_pf_2
	s_waitcnt vmcnt(0)
	s_branch .LBB0_658
.Lret_pf_2:
	s_lshl_b32 s0, s92, 4
	s_and_b32 vcc_lo, s0, 0xffffff80
	s_ashr_i32 vcc_hi, vcc_lo, 31
	s_lshl_b64 s[36:37], vcc, 11
	v_readlane_b32 s0, v252, 47
	s_add_u32 s35, s0, s36
	v_readlane_b32 s0, v252, 49
	s_addc_u32 s39, s0, s37
	s_lshl_b32 s0, s92, 8
	s_and_b32 s0, s0, 0x700
	s_add_u32 s38, s35, s0
	s_addc_u32 s39, s39, 0
	v_readlane_b32 s35, v252, 51
	s_add_u32 s35, s35, s36
	v_readlane_b32 s36, v252, 29
	v_or_b32_e32 v34, vcc_lo, v1
	s_addc_u32 s37, s36, s37
	v_ashrrev_i32_e32 v35, 31, v34
	s_add_u32 s36, s35, s0
	v_lshlrev_b64 v[34:35], 11, v[34:35]
	s_addc_u32 s37, s37, 0
	v_mov_b32_e32 v109, v99
	v_mov_b32_e32 v111, v99
	v_lshl_add_u64 v[34:35], s[4:5], 0, v[34:35]
	v_lshl_add_u64 v[26:27], s[38:39], 0, v[108:109]
	v_lshl_add_u64 v[28:29], s[36:37], 0, v[110:111]
	v_mov_b32_e32 v113, v99
	v_mov_b32_e32 v115, v99
	v_mov_b32_e32 v117, v99
	v_mov_b32_e32 v119, v99
	v_mov_b32_e32 v121, v99
	v_mov_b32_e32 v123, v99
	v_mov_b32_e32 v125, v99
	v_mov_b32_e32 v127, v99
	v_lshl_add_u64 v[34:35], v[34:35], 0, s[0:1]
	v_mov_b32_e32 v129, v99
	v_lshl_add_u64 v[2:3], v[26:27], 0, v[112:113]
	v_lshl_add_u64 v[6:7], v[28:29], 0, v[114:115]
	v_lshl_add_u64 v[10:11], v[26:27], 0, v[116:117]
	v_lshl_add_u64 v[14:15], v[28:29], 0, v[118:119]
	v_lshl_add_u64 v[18:19], v[26:27], 0, v[120:121]
	v_lshl_add_u64 v[22:23], v[28:29], 0, v[122:123]
	v_lshl_add_u64 v[26:27], v[26:27], 0, v[124:125]
	v_lshl_add_u64 v[30:31], v[28:29], 0, v[126:127]
	v_lshl_add_u64 v[46:47], v[34:35], 0, v[128:129]
	global_load_dwordx4 v[2:5], v[2:3], off
	s_nop 0
	global_load_dwordx4 v[6:9], v[6:7], off
	s_nop 0
	global_load_dwordx4 v[10:13], v[10:11], off
	s_nop 0
	global_load_dwordx4 v[14:17], v[14:15], off
	s_nop 0
	global_load_dwordx4 v[18:21], v[18:19], off
	s_nop 0
	global_load_dwordx4 v[22:25], v[22:23], off
	s_nop 0
	global_load_dwordx4 v[26:29], v[26:27], off
	s_nop 0
	global_load_dwordx4 v[30:33], v[30:31], off
	s_nop 0
	global_load_dwordx4 v[34:37], v[46:47], off
	global_load_dwordx4 v[38:41], v[46:47], off offset:64
	global_load_dwordx4 v[42:45], v[46:47], off offset:128
	s_nop 0
	global_load_dwordx4 v[46:49], v[46:47], off offset:192

.LBB0_712:
	s_and_saveexec_b64 vcc, s[74:75]
	ds_write_b32 v156, v82 offset:228
	s_or_b64 exec, exec, vcc
	v_add_u32_e32 v82, v149, v152
	s_waitcnt vmcnt(15)
	ds_write_b128 v82, v[70:73]
	v_add_u32_e32 v70, v149, v153
	s_waitcnt vmcnt(14)
	ds_write_b128 v70, v[66:69]
	s_waitcnt vmcnt(13)
	ds_write_b128 v82, v[78:81] offset:17408
	v_add_u32_e32 v66, v149, v154
	s_waitcnt vmcnt(12)
	ds_write_b128 v66, v[74:77]
	v_mov_b32_e32 v66, 0
	s_lshl_b32 s0, s88, 7
	v_mov_b32_e32 v105, v191
	v_mov_b32_e32 v107, v190
	s_mov_b32 s74, s33
	v_mov_b32_e32 v67, v66
	v_mov_b32_e32 v68, v66
	v_mov_b32_e32 v69, v66
	v_mov_b32_e32 v70, v66
	v_mov_b32_e32 v71, v66
	v_mov_b32_e32 v72, v66
	v_mov_b32_e32 v73, v66
	v_mov_b32_e32 v74, v66
	v_mov_b32_e32 v75, v66
	v_mov_b32_e32 v76, v66
	v_mov_b32_e32 v77, v66
	v_mov_b32_e32 v78, v66
	v_mov_b32_e32 v79, v66
	v_mov_b32_e32 v80, v66
	v_mov_b32_e32 v81, v66
	v_mov_b32_e32 v82, v66
	v_mov_b32_e32 v83, v66
	v_mov_b32_e32 v84, v66
	v_mov_b32_e32 v85, v66
	v_mov_b32_e32 v86, v66
	v_mov_b32_e32 v87, v66
	v_mov_b32_e32 v88, v66
	v_mov_b32_e32 v89, v66
	v_mov_b32_e32 v90, v66
	v_mov_b32_e32 v91, v66
	v_mov_b32_e32 v92, v66
	v_mov_b32_e32 v93, v66
	v_mov_b32_e32 v94, v66
	v_mov_b32_e32 v95, v66
	v_mov_b32_e32 v96, v66
	v_mov_b32_e32 v97, v66
	s_waitcnt lgkmcnt(0)
	s_barrier
.LBB0_715:
	ds_read_b128 v[206:209], v105
	ds_read_b128 v[210:213], v107
	s_waitcnt lgkmcnt(0)
	v_mfma_f32_16x16x32_bf16 v[94:97], v[210:213], v[206:209], v[94:97]
	ds_read_b128 v[210:213], v107 offset:4352
	s_waitcnt lgkmcnt(0)
	v_mfma_f32_16x16x32_bf16 v[90:93], v[210:213], v[206:209], v[90:93]
	ds_read_b128 v[210:213], v107 offset:8704
	s_waitcnt lgkmcnt(0)
	v_mfma_f32_16x16x32_bf16 v[86:89], v[210:213], v[206:209], v[86:89]
	ds_read_b128 v[210:213], v107 offset:13056
	s_waitcnt lgkmcnt(0)
	v_mfma_f32_16x16x32_bf16 v[82:85], v[210:213], v[206:209], v[82:85]
	ds_read_b128 v[210:213], v107 offset:17408
	s_waitcnt lgkmcnt(0)
	v_mfma_f32_16x16x32_bf16 v[78:81], v[210:213], v[206:209], v[78:81]
	ds_read_b128 v[210:213], v107 offset:21760
	s_waitcnt lgkmcnt(0)
	v_mfma_f32_16x16x32_bf16 v[74:77], v[210:213], v[206:209], v[74:77]
	ds_read_b128 v[210:213], v107 offset:26112
	s_waitcnt lgkmcnt(0)
	v_mfma_f32_16x16x32_bf16 v[70:73], v[210:213], v[206:209], v[70:73]
	ds_read_b128 v[210:213], v107 offset:30464
	s_waitcnt lgkmcnt(0)
	v_mfma_f32_16x16x32_bf16 v[66:69], v[210:213], v[206:209], v[66:69]
	s_add_i32 s74, s74, -1
	v_add_u32_e32 v107, 64, v107
	s_cmp_lg_u32 s74, 0
	v_add_u32_e32 v105, 64, v105
	s_cbranch_scc1 .LBB0_715
	ds_read_b128 v[206:209], v194
	ds_read_b128 v[210:213], v194 offset:4352
	ds_read_b128 v[214:217], v194 offset:8704
	ds_read_b128 v[218:221], v194 offset:13056
	ds_read_b128 v[222:225], v194 offset:17408
	ds_read_b128 v[226:229], v194 offset:21760
	ds_read_b128 v[230:233], v194 offset:26112
	ds_read_b128 v[234:237], v194 offset:30464
	s_waitcnt lgkmcnt(7)
	v_mfma_f32_16x16x32_bf16 v[206:209], v[206:209], v[62:65], 0
	s_waitcnt lgkmcnt(6)
	v_mfma_f32_16x16x32_bf16 v[210:213], v[210:213], v[62:65], 0
	s_waitcnt lgkmcnt(5)
	v_mfma_f32_16x16x32_bf16 v[214:217], v[214:217], v[62:65], 0
	s_waitcnt lgkmcnt(4)
	v_mfma_f32_16x16x32_bf16 v[218:221], v[218:221], v[62:65], 0
	s_waitcnt lgkmcnt(3)
	v_mfma_f32_16x16x32_bf16 v[222:225], v[222:225], v[62:65], 0
	s_waitcnt lgkmcnt(2)
	v_mfma_f32_16x16x32_bf16 v[226:229], v[226:229], v[62:65], 0
	s_waitcnt lgkmcnt(1)
	v_mfma_f32_16x16x32_bf16 v[230:233], v[230:233], v[62:65], 0
	s_waitcnt lgkmcnt(0)
	v_mfma_f32_16x16x32_bf16 v[62:65], v[234:237], v[62:65], 0
	ds_read_b128 v[234:237], v194 offset:64
	s_waitcnt lgkmcnt(0)
	v_mfma_f32_16x16x32_bf16 v[206:209], v[234:237], v[58:61], v[206:209]
	ds_read_b128 v[234:237], v194 offset:4416
	s_waitcnt lgkmcnt(0)
	v_mfma_f32_16x16x32_bf16 v[210:213], v[234:237], v[58:61], v[210:213]
	ds_read_b128 v[234:237], v194 offset:8768
	s_waitcnt lgkmcnt(0)
	v_mfma_f32_16x16x32_bf16 v[214:217], v[234:237], v[58:61], v[214:217]
	ds_read_b128 v[234:237], v194 offset:13120
	s_waitcnt lgkmcnt(0)
	v_mfma_f32_16x16x32_bf16 v[218:221], v[234:237], v[58:61], v[218:221]
	ds_read_b128 v[234:237], v194 offset:17472
	s_waitcnt lgkmcnt(0)
	v_mfma_f32_16x16x32_bf16 v[222:225], v[234:237], v[58:61], v[222:225]
	ds_read_b128 v[234:237], v194 offset:21824
	s_waitcnt lgkmcnt(0)
	v_mfma_f32_16x16x32_bf16 v[226:229], v[234:237], v[58:61], v[226:229]
	ds_read_b128 v[234:237], v194 offset:26176
	s_waitcnt lgkmcnt(0)
	v_mfma_f32_16x16x32_bf16 v[230:233], v[234:237], v[58:61], v[230:233]
	ds_read_b128 v[234:237], v194 offset:30528
	s_waitcnt lgkmcnt(0)
	v_mfma_f32_16x16x32_bf16 v[58:61], v[234:237], v[58:61], v[62:65]
	s_nop 2
	ds_read_b128 v[62:65], v194 offset:128
	s_waitcnt lgkmcnt(0)
	v_mfma_f32_16x16x32_bf16 v[62:65], v[62:65], v[54:57], v[206:209]
	s_nop 2
	ds_read_b128 v[206:209], v194 offset:4480
	s_waitcnt lgkmcnt(0)
	v_mfma_f32_16x16x32_bf16 v[206:209], v[206:209], v[54:57], v[210:213]
	s_nop 2
	ds_read_b128 v[210:213], v194 offset:8832
	s_waitcnt lgkmcnt(0)
	v_mfma_f32_16x16x32_bf16 v[210:213], v[210:213], v[54:57], v[214:217]
	s_nop 2
	ds_read_b128 v[214:217], v194 offset:13184
	s_waitcnt lgkmcnt(0)
	v_mfma_f32_16x16x32_bf16 v[214:217], v[214:217], v[54:57], v[218:221]
	s_nop 2
	ds_read_b128 v[218:221], v194 offset:17536
	s_waitcnt lgkmcnt(0)
	v_mfma_f32_16x16x32_bf16 v[218:221], v[218:221], v[54:57], v[222:225]
	s_nop 2
	ds_read_b128 v[222:225], v194 offset:21888
	s_waitcnt lgkmcnt(0)
	v_mfma_f32_16x16x32_bf16 v[222:225], v[222:225], v[54:57], v[226:229]
	s_nop 2
	ds_read_b128 v[226:229], v194 offset:26240
	s_waitcnt lgkmcnt(0)
	v_mfma_f32_16x16x32_bf16 v[226:229], v[226:229], v[54:57], v[230:233]
	s_nop 2
	ds_read_b128 v[230:233], v194 offset:30592
	s_waitcnt lgkmcnt(0)
	v_mfma_f32_16x16x32_bf16 v[54:57], v[230:233], v[54:57], v[58:61]
	s_nop 2
	ds_read_b128 v[58:61], v194 offset:192
	s_waitcnt lgkmcnt(0)
	v_mfma_f32_16x16x32_bf16 v[58:61], v[58:61], v[50:53], v[62:65]
	s_nop 2
	ds_read_b128 v[62:65], v194 offset:4544
	s_waitcnt lgkmcnt(0)
	v_mfma_f32_16x16x32_bf16 v[62:65], v[62:65], v[50:53], v[206:209]
	s_nop 2
	ds_read_b128 v[206:209], v194 offset:8896
	s_waitcnt lgkmcnt(0)
	v_mfma_f32_16x16x32_bf16 v[206:209], v[206:209], v[50:53], v[210:213]
	s_nop 2
	ds_read_b128 v[210:213], v194 offset:13248
	s_waitcnt lgkmcnt(0)
	v_mfma_f32_16x16x32_bf16 v[210:213], v[210:213], v[50:53], v[214:217]
	s_nop 2
	ds_read_b128 v[214:217], v194 offset:17600
	s_waitcnt lgkmcnt(0)
	v_mfma_f32_16x16x32_bf16 v[214:217], v[214:217], v[50:53], v[218:221]
	s_nop 2
	ds_read_b128 v[218:221], v194 offset:21952
	s_waitcnt lgkmcnt(0)
	v_mfma_f32_16x16x32_bf16 v[218:221], v[218:221], v[50:53], v[222:225]
	s_nop 2
	ds_read_b128 v[222:225], v194 offset:26304
	s_waitcnt lgkmcnt(0)
	v_mfma_f32_16x16x32_bf16 v[222:225], v[222:225], v[50:53], v[226:229]
	s_nop 2
	ds_read_b128 v[226:229], v194 offset:30656
	s_waitcnt lgkmcnt(0)
	v_mfma_f32_16x16x32_bf16 v[226:229], v[226:229], v[50:53], v[54:57]
	v_mul_f32_e32 v50, v103, v157
	v_cmp_gt_f32_e32 vcc, s89, v50
	s_mov_b32 s34, 0xf800000
	s_lshl_b32 s0, s0, 1
	v_cndmask_b32_e32 v51, 0, v200, vcc
	v_fmac_f32_e32 v51, v103, v157
	v_exp_f32_e32 v51, v51
	v_cndmask_b32_e32 v50, 0, v203, vcc
	v_ldexp_f32 v52, v51, v50
	v_pk_fma_f32 v[94:95], v[52:53], v[58:59], v[94:95] op_sel_hi:[0,1,1]
	v_pk_fma_f32 v[90:91], v[52:53], v[62:63], v[90:91] op_sel_hi:[0,1,1]
	v_pk_fma_f32 v[96:97], v[52:53], v[60:61], v[96:97] op_sel_hi:[0,1,1]
	v_pk_fma_f32 v[92:93], v[52:53], v[64:65], v[92:93] op_sel_hi:[0,1,1]
	v_mov_b32_e32 v50, v94
	v_mov_b32_e32 v51, v90
	v_mov_b32_e32 v54, v95
	v_mov_b32_e32 v55, v91
	v_pk_add_f32 v[50:51], v[50:51], v[54:55]
	v_mov_b32_e32 v54, v96
	v_mov_b32_e32 v55, v92
	v_mov_b32_e32 v56, v97
	v_mov_b32_e32 v57, v93
	v_pk_add_f32 v[54:55], v[54:55], v[56:57]
	v_pk_fma_f32 v[86:87], v[52:53], v[206:207], v[86:87] op_sel_hi:[0,1,1]
	v_pk_fma_f32 v[88:89], v[52:53], v[208:209], v[88:89] op_sel_hi:[0,1,1]
	v_pk_add_f32 v[50:51], v[50:51], v[54:55]
	v_pk_mov_b32 v[54:55], v[86:87], v[88:89] op_sel:[1,0]
	v_mov_b32_e32 v56, v86
	v_mov_b32_e32 v57, v89
	v_pk_add_f32 v[54:55], v[54:55], v[56:57]
	v_add_f32_e32 v50, 0, v50
	v_pk_add_f32 v[54:55], v[54:55], v[54:55] op_sel:[0,1] op_sel_hi:[1,0]
	v_pk_fma_f32 v[84:85], v[52:53], v[212:213], v[84:85] op_sel_hi:[0,1,1]
	v_pk_fma_f32 v[82:83], v[52:53], v[210:211], v[82:83] op_sel_hi:[0,1,1]
	v_pk_fma_f32 v[62:63], v[52:53], v[216:217], v[80:81] op_sel_hi:[0,1,1]
	v_pk_fma_f32 v[64:65], v[52:53], v[214:215], v[78:79] op_sel_hi:[0,1,1]
	v_add_f32_e32 v50, v50, v51
	v_add_f32_e32 v56, v82, v83
	v_add_f32_e32 v58, v84, v85
	v_mov_b32_e32 v51, v64
	v_mov_b32_e32 v55, v65
	v_mov_b32_e32 v57, v62
	v_mov_b32_e32 v59, v63
	v_pk_add_f32 v[50:51], v[50:51], v[54:55]
	v_pk_add_f32 v[54:55], v[56:57], v[58:59]
	v_pk_fma_f32 v[58:59], v[52:53], v[218:219], v[74:75] op_sel_hi:[0,1,1]
	v_pk_add_f32 v[50:51], v[50:51], v[54:55]
	v_pk_fma_f32 v[60:61], v[52:53], v[220:221], v[76:77] op_sel_hi:[0,1,1]
	v_pk_add_f32 v[78:79], v[50:51], v[50:51] op_sel:[0,1] op_sel_hi:[1,0]
	v_pk_mov_b32 v[50:51], v[58:59], v[60:61] op_sel:[1,0]
	v_mov_b32_e32 v54, v58
	v_mov_b32_e32 v55, v61
	v_pk_add_f32 v[50:51], v[50:51], v[54:55]
	v_pk_fma_f32 v[54:55], v[52:53], v[224:225], v[72:73] op_sel_hi:[0,1,1]
	v_pk_add_f32 v[74:75], v[50:51], v[50:51] op_sel:[0,1] op_sel_hi:[1,0]
	v_pk_fma_f32 v[56:57], v[52:53], v[222:223], v[70:71] op_sel_hi:[0,1,1]
	v_pk_fma_f32 v[50:51], v[52:53], v[228:229], v[68:69] op_sel_hi:[0,1,1]
	v_pk_fma_f32 v[52:53], v[52:53], v[226:227], v[66:67] op_sel_hi:[0,1,1]
	v_add_f32_e32 v70, v56, v57
	v_add_f32_e32 v72, v54, v55
	v_mov_b32_e32 v79, v52
	v_mov_b32_e32 v75, v53
	v_mov_b32_e32 v71, v50
	v_mov_b32_e32 v73, v51
	v_pk_add_f32 v[66:67], v[78:79], v[74:75]
	v_pk_add_f32 v[68:69], v[70:71], v[72:73]
	s_nop 0
	v_pk_add_f32 v[66:67], v[66:67], v[68:69]
	s_nop 0
	v_add_f32_e32 v66, v66, v67
	ds_bpermute_b32 v67, v150, v66
	s_waitcnt lgkmcnt(0)
	v_add_f32_e32 v66, v66, v67
	ds_bpermute_b32 v67, v151, v66
	s_waitcnt lgkmcnt(0)
	v_add_f32_e32 v103, v66, v67
	v_fmamk_f32 v70, v103, 0xbc000000, v97
	v_fmamk_f32 v72, v103, 0xbc000000, v95
	v_fmamk_f32 v71, v103, 0xbc000000, v93
	v_fmac_f32_e32 v92, 0xbc000000, v103
	v_fmamk_f32 v73, v103, 0xbc000000, v91
	v_fmac_f32_e32 v90, 0xbc000000, v103
	v_fmac_f32_e32 v96, 0xbc000000, v103
	v_fmac_f32_e32 v94, 0xbc000000, v103
	v_mov_b32_e32 v95, v90
	v_pk_mul_f32 v[66:67], v[72:73], v[72:73]
	v_mov_b32_e32 v97, v92
	v_pk_mul_f32 v[68:69], v[70:71], v[70:71]
	v_pk_fma_f32 v[66:67], v[94:95], v[94:95], v[66:67]
	v_pk_fma_f32 v[68:69], v[96:97], v[96:97], v[68:69]
	v_fmamk_f32 v87, v103, 0xbc000000, v87
	v_pk_add_f32 v[66:67], v[66:67], v[68:69]
	v_fmac_f32_e32 v86, 0xbc000000, v103
	v_fmamk_f32 v89, v103, 0xbc000000, v89
	v_fmac_f32_e32 v88, 0xbc000000, v103
	v_pk_add_f32 v[66:67], v[66:67], v[66:67] op_sel_hi:[0,1]
	v_pk_mul_f32 v[68:69], v[88:89], v[88:89]
	v_pk_mul_f32 v[74:75], v[86:87], v[86:87]
	v_fmac_f32_e32 v82, 0xbc000000, v103
	v_pk_mov_b32 v[76:77], v[74:75], v[68:69] op_sel:[1,0]
	v_mov_b32_e32 v75, v69
	v_fmamk_f32 v83, v103, 0xbc000000, v83
	v_fmac_f32_e32 v84, 0xbc000000, v103
	v_mul_f32_e32 v66, v82, v82
	v_pk_add_f32 v[68:69], v[76:77], v[74:75]
	v_fmamk_f32 v85, v103, 0xbc000000, v85
	v_pk_fma_f32 v[76:77], v[82:83], v[82:83], v[66:67] op_sel_hi:[1,1,0]
	v_mul_f32_e32 v66, v84, v84
	v_pk_add_f32 v[74:75], v[68:69], v[68:69] op_sel_hi:[0,1]
	v_pk_fma_f32 v[78:79], v[84:85], v[84:85], v[66:67] op_sel_hi:[1,1,0]
	v_fmamk_f32 v69, v103, 0xbc000000, v63
	v_fmac_f32_e32 v62, 0xbc000000, v103
	v_fmamk_f32 v68, v103, 0xbc000000, v65
	v_fmac_f32_e32 v64, 0xbc000000, v103
	v_mul_f32_e32 v76, v64, v64
	v_mul_f32_e32 v78, v68, v68
	v_mul_f32_e32 v74, v62, v62
	v_mul_f32_e32 v66, v69, v69
	v_pk_add_f32 v[76:77], v[76:77], v[78:79]
	v_pk_add_f32 v[66:67], v[74:75], v[66:67]
	v_fmamk_f32 v59, v103, 0xbc000000, v59
	v_pk_add_f32 v[66:67], v[76:77], v[66:67]
	v_fmac_f32_e32 v58, 0xbc000000, v103
	v_fmamk_f32 v61, v103, 0xbc000000, v61
	v_fmac_f32_e32 v60, 0xbc000000, v103
	v_pk_add_f32 v[74:75], v[66:67], v[66:67] op_sel_hi:[0,1]
	v_pk_mul_f32 v[66:67], v[60:61], v[60:61]
	v_pk_mul_f32 v[76:77], v[58:59], v[58:59]
	v_fmac_f32_e32 v56, 0xbc000000, v103
	v_pk_mov_b32 v[78:79], v[76:77], v[66:67] op_sel:[1,0]
	v_mov_b32_e32 v77, v67
	v_pk_add_f32 v[66:67], v[78:79], v[76:77]
	v_fmamk_f32 v57, v103, 0xbc000000, v57
	v_pk_add_f32 v[76:77], v[66:67], v[66:67] op_sel_hi:[0,1]
	v_fmac_f32_e32 v54, 0xbc000000, v103
	v_mul_f32_e32 v66, v56, v56
	v_fmamk_f32 v55, v103, 0xbc000000, v55
	v_pk_fma_f32 v[78:79], v[56:57], v[56:57], v[66:67] op_sel_hi:[1,1,0]
	v_mul_f32_e32 v66, v54, v54
	v_pk_fma_f32 v[80:81], v[54:55], v[54:55], v[66:67] op_sel_hi:[1,1,0]
	v_fmamk_f32 v67, v103, 0xbc000000, v51
	v_fmac_f32_e32 v50, 0xbc000000, v103
	v_fmamk_f32 v66, v103, 0xbc000000, v53
	v_fmac_f32_e32 v52, 0xbc000000, v103
	v_mul_f32_e32 v78, v52, v52
	v_mul_f32_e32 v80, v66, v66
	v_mul_f32_e32 v76, v50, v50
	v_mul_f32_e32 v74, v67, v67
	v_pk_add_f32 v[78:79], v[78:79], v[80:81]
	v_pk_add_f32 v[74:75], v[76:77], v[74:75]
	v_mov_b32_e32 v95, v96
	v_pk_add_f32 v[74:75], v[78:79], v[74:75]
	v_lshlrev_b32_e32 v81, 16, v145
	v_add_f32_e32 v51, v74, v75
	ds_bpermute_b32 v53, v150, v51
	v_lshlrev_b32_e32 v80, 16, v144
	v_lshlrev_b64 v[76:77], 12, v[146:147]
	v_lshl_add_u64 v[76:77], s[78:79], 0, v[76:77]
	v_lshl_add_u64 v[76:77], v[76:77], 0, s[0:1]
	s_waitcnt lgkmcnt(0)
	v_add_f32_e32 v51, v51, v53
	ds_bpermute_b32 v53, v151, v51
	v_lshl_add_u64 v[76:77], v[76:77], 0, v[98:99]
	v_mov_b32_e32 v91, v92
	s_waitcnt lgkmcnt(0)
	v_add_f32_e32 v51, v51, v53
	v_fmamk_f32 v51, v51, 0x3c000000, v197
	v_mul_f32_e32 v53, 0x4f800000, v51
	v_cmp_gt_f32_e32 vcc, s34, v51
	s_nop 1
	v_cndmask_b32_e32 v51, v51, v53, vcc
	v_sqrt_f32_e32 v53, v51
	s_nop 0
	v_add_u32_e32 v63, -1, v53
	v_fma_f32 v65, -v63, v53, v51
	v_cmp_ge_f32_e64 s[74:75], 0, v65
	v_add_u32_e32 v65, 1, v53
	s_nop 0
	v_cndmask_b32_e64 v63, v53, v63, s[74:75]
	v_fma_f32 v53, -v65, v53, v51
	v_cmp_lt_f32_e64 s[74:75], 0, v53
	s_nop 1
	v_cndmask_b32_e64 v53, v63, v65, s[74:75]
	v_mul_f32_e32 v63, 0x37800000, v53
	v_cndmask_b32_e32 v53, v53, v63, vcc
	v_cmp_class_f32_e32 vcc, v51, v199
	s_nop 1
	v_cndmask_b32_e32 v51, v53, v51, vcc
	v_div_scale_f32 v53, s[34:35], v51, v51, 1.0
	v_rcp_f32_e32 v63, v53
	s_nop 0
	v_fma_f32 v65, -v53, v63, 1.0
	v_fmac_f32_e32 v63, v65, v63
	v_div_scale_f32 v65, vcc, 1.0, v51, 1.0
	v_mul_f32_e32 v74, v65, v63
	v_fma_f32 v75, -v53, v74, v65
	v_fmac_f32_e32 v74, v75, v63
	v_fma_f32 v53, -v53, v74, v65
	v_div_fmas_f32 v53, v53, v63, v74
	v_div_fixup_f32 v74, v53, v51, 1.0
	v_pk_mul_f32 v[78:79], v[94:95], v[74:75] op_sel_hi:[1,0]
	v_and_b32_e32 v95, 0xffff0000, v145
	v_pk_mul_f32 v[78:79], v[78:79], v[80:81]
	v_mov_b32_e32 v80, v72
	v_mov_b32_e32 v81, v70
	v_pk_mul_f32 v[80:81], v[80:81], v[74:75] op_sel_hi:[1,0]
	v_and_b32_e32 v94, 0xffff0000, v144
	v_pk_mul_f32 v[80:81], v[80:81], v[94:95]
	v_and_b32_sdwa v51, v79, v204 dst_sel:DWORD dst_unused:UNUSED_PAD src0_sel:WORD_1 src1_sel:DWORD
	v_and_b32_sdwa v63, v81, v204 dst_sel:DWORD dst_unused:UNUSED_PAD src0_sel:WORD_1 src1_sel:DWORD
	v_and_b32_sdwa v65, v80, v204 dst_sel:DWORD dst_unused:UNUSED_PAD src0_sel:WORD_1 src1_sel:DWORD
	v_and_b32_sdwa v53, v78, v204 dst_sel:DWORD dst_unused:UNUSED_PAD src0_sel:WORD_1 src1_sel:DWORD
	v_add3_u32 v63, v81, v63, s2
	v_add3_u32 v65, v80, v65, s2
	v_add3_u32 v53, v78, v53, s2
	v_add3_u32 v51, v79, v51, s2
	v_and_b32_e32 v63, 0xffff0000, v63
	v_and_b32_e32 v65, 0xffff0000, v65
	v_mov_b32_e32 v70, v73
	v_or_b32_sdwa v79, v63, v51 dst_sel:DWORD dst_unused:UNUSED_PAD src0_sel:DWORD src1_sel:WORD_1
	v_or_b32_sdwa v78, v65, v53 dst_sel:DWORD dst_unused:UNUSED_PAD src0_sel:DWORD src1_sel:WORD_1
	v_pk_mul_f32 v[70:71], v[70:71], v[74:75] op_sel_hi:[1,0]
	v_and_b32_e32 v73, 0xffff0000, v143
	v_and_b32_e32 v72, 0xffff0000, v142
	global_store_dwordx2 v[76:77], v[78:79], off offset:2048
	v_pk_mul_f32 v[78:79], v[90:91], v[74:75] op_sel_hi:[1,0]
	v_lshlrev_b32_e32 v81, 16, v143
	v_lshlrev_b32_e32 v80, 16, v142
	v_pk_mul_f32 v[70:71], v[70:71], v[72:73]
	v_pk_mul_f32 v[78:79], v[78:79], v[80:81]
	v_and_b32_sdwa v63, v71, v204 dst_sel:DWORD dst_unused:UNUSED_PAD src0_sel:WORD_1 src1_sel:DWORD
	v_and_b32_sdwa v65, v70, v204 dst_sel:DWORD dst_unused:UNUSED_PAD src0_sel:WORD_1 src1_sel:DWORD
	v_and_b32_sdwa v51, v79, v204 dst_sel:DWORD dst_unused:UNUSED_PAD src0_sel:WORD_1 src1_sel:DWORD
	v_and_b32_sdwa v53, v78, v204 dst_sel:DWORD dst_unused:UNUSED_PAD src0_sel:WORD_1 src1_sel:DWORD
	v_add3_u32 v63, v71, v63, s2
	v_add3_u32 v65, v70, v65, s2
	v_add3_u32 v53, v78, v53, s2
	v_add3_u32 v51, v79, v51, s2
	v_and_b32_e32 v63, 0xffff0000, v63
	v_and_b32_e32 v65, 0xffff0000, v65
	v_or_b32_sdwa v71, v63, v51 dst_sel:DWORD dst_unused:UNUSED_PAD src0_sel:DWORD src1_sel:WORD_1
	v_or_b32_sdwa v70, v65, v53 dst_sel:DWORD dst_unused:UNUSED_PAD src0_sel:DWORD src1_sel:WORD_1
	global_store_dwordx2 v[76:77], v[70:71], off offset:2080
	v_mov_b32_e32 v70, v86
	v_mov_b32_e32 v71, v88
	v_pk_mul_f32 v[70:71], v[70:71], v[74:75] op_sel_hi:[1,0]
	v_lshlrev_b32_e32 v73, 16, v141
	v_lshlrev_b32_e32 v72, 16, v140
	v_mov_b32_e32 v88, v87
	v_pk_mul_f32 v[70:71], v[70:71], v[72:73]
	v_pk_mul_f32 v[72:73], v[88:89], v[74:75] op_sel_hi:[1,0]
	v_and_b32_e32 v79, 0xffff0000, v141
	v_and_b32_e32 v78, 0xffff0000, v140
	v_pk_mul_f32 v[72:73], v[72:73], v[78:79]
	v_and_b32_sdwa v51, v71, v204 dst_sel:DWORD dst_unused:UNUSED_PAD src0_sel:WORD_1 src1_sel:DWORD
	v_and_b32_sdwa v63, v73, v204 dst_sel:DWORD dst_unused:UNUSED_PAD src0_sel:WORD_1 src1_sel:DWORD
	v_and_b32_sdwa v65, v72, v204 dst_sel:DWORD dst_unused:UNUSED_PAD src0_sel:WORD_1 src1_sel:DWORD
	v_and_b32_sdwa v53, v70, v204 dst_sel:DWORD dst_unused:UNUSED_PAD src0_sel:WORD_1 src1_sel:DWORD
	v_add3_u32 v63, v73, v63, s2
	v_add3_u32 v65, v72, v65, s2
	v_add3_u32 v53, v70, v53, s2
	v_add3_u32 v51, v71, v51, s2
	v_and_b32_e32 v63, 0xffff0000, v63
	v_and_b32_e32 v65, 0xffff0000, v65
	v_or_b32_sdwa v71, v63, v51 dst_sel:DWORD dst_unused:UNUSED_PAD src0_sel:DWORD src1_sel:WORD_1
	v_or_b32_sdwa v70, v65, v53 dst_sel:DWORD dst_unused:UNUSED_PAD src0_sel:DWORD src1_sel:WORD_1
	global_store_dwordx2 v[76:77], v[70:71], off offset:2112
	v_mov_b32_e32 v70, v82
	v_mov_b32_e32 v71, v84
	v_pk_mul_f32 v[70:71], v[70:71], v[74:75] op_sel_hi:[1,0]
	v_lshlrev_b32_e32 v73, 16, v139
	v_lshlrev_b32_e32 v72, 16, v138
	v_mov_b32_e32 v84, v83
	v_pk_mul_f32 v[70:71], v[70:71], v[72:73]
	v_pk_mul_f32 v[72:73], v[84:85], v[74:75] op_sel_hi:[1,0]
	v_and_b32_e32 v79, 0xffff0000, v139
	v_and_b32_e32 v78, 0xffff0000, v138
	v_pk_mul_f32 v[72:73], v[72:73], v[78:79]
	v_and_b32_sdwa v53, v70, v204 dst_sel:DWORD dst_unused:UNUSED_PAD src0_sel:WORD_1 src1_sel:DWORD
	v_and_b32_sdwa v65, v72, v204 dst_sel:DWORD dst_unused:UNUSED_PAD src0_sel:WORD_1 src1_sel:DWORD
	v_and_b32_sdwa v63, v73, v204 dst_sel:DWORD dst_unused:UNUSED_PAD src0_sel:WORD_1 src1_sel:DWORD
	v_add3_u32 v65, v72, v65, s2
	v_and_b32_sdwa v51, v71, v204 dst_sel:DWORD dst_unused:UNUSED_PAD src0_sel:WORD_1 src1_sel:DWORD
	v_add3_u32 v53, v70, v53, s2
	v_add3_u32 v63, v73, v63, s2
	v_and_b32_e32 v65, 0xffff0000, v65
	v_add3_u32 v51, v71, v51, s2
	v_and_b32_e32 v63, 0xffff0000, v63
	v_or_b32_sdwa v70, v65, v53 dst_sel:DWORD dst_unused:UNUSED_PAD src0_sel:DWORD src1_sel:WORD_1
	v_mov_b32_e32 v65, v62
	v_or_b32_sdwa v71, v63, v51 dst_sel:DWORD dst_unused:UNUSED_PAD src0_sel:DWORD src1_sel:WORD_1
	v_pk_mul_f32 v[62:63], v[64:65], v[74:75] op_sel_hi:[1,0]
	v_lshlrev_b32_e32 v65, 16, v137
	v_lshlrev_b32_e32 v64, 16, v136
	v_pk_mul_f32 v[62:63], v[62:63], v[64:65]
	v_pk_mul_f32 v[64:65], v[68:69], v[74:75] op_sel_hi:[1,0]
	v_and_b32_e32 v69, 0xffff0000, v137
	v_and_b32_e32 v68, 0xffff0000, v136
	v_pk_mul_f32 v[64:65], v[64:65], v[68:69]
	v_and_b32_sdwa v51, v63, v204 dst_sel:DWORD dst_unused:UNUSED_PAD src0_sel:WORD_1 src1_sel:DWORD
	v_and_b32_sdwa v53, v62, v204 dst_sel:DWORD dst_unused:UNUSED_PAD src0_sel:WORD_1 src1_sel:DWORD
	v_add3_u32 v53, v62, v53, s2
	v_add3_u32 v51, v63, v51, s2
	v_and_b32_sdwa v62, v65, v204 dst_sel:DWORD dst_unused:UNUSED_PAD src0_sel:WORD_1 src1_sel:DWORD
	v_and_b32_sdwa v63, v64, v204 dst_sel:DWORD dst_unused:UNUSED_PAD src0_sel:WORD_1 src1_sel:DWORD
	v_add3_u32 v62, v65, v62, s2
	v_add3_u32 v63, v64, v63, s2
	v_and_b32_e32 v62, 0xffff0000, v62
	v_and_b32_e32 v64, 0xffff0000, v63
	v_or_b32_sdwa v63, v62, v51 dst_sel:DWORD dst_unused:UNUSED_PAD src0_sel:DWORD src1_sel:WORD_1
	v_or_b32_sdwa v62, v64, v53 dst_sel:DWORD dst_unused:UNUSED_PAD src0_sel:DWORD src1_sel:WORD_1
	global_store_dwordx2 v[76:77], v[62:63], off offset:2176
	v_mov_b32_e32 v63, v60
	v_mov_b32_e32 v60, v59
	v_mov_b32_e32 v62, v58
	v_pk_mul_f32 v[58:59], v[60:61], v[74:75] op_sel_hi:[1,0]
	v_and_b32_e32 v61, 0xffff0000, v135
	v_and_b32_e32 v60, 0xffff0000, v134
	v_pk_mul_f32 v[62:63], v[62:63], v[74:75] op_sel_hi:[1,0]
	v_lshlrev_b32_e32 v65, 16, v135
	v_lshlrev_b32_e32 v64, 16, v134
	v_pk_mul_f32 v[58:59], v[58:59], v[60:61]
	v_pk_mul_f32 v[62:63], v[62:63], v[64:65]
	v_and_b32_sdwa v60, v59, v204 dst_sel:DWORD dst_unused:UNUSED_PAD src0_sel:WORD_1 src1_sel:DWORD
	v_and_b32_sdwa v61, v58, v204 dst_sel:DWORD dst_unused:UNUSED_PAD src0_sel:WORD_1 src1_sel:DWORD
	v_and_b32_sdwa v51, v63, v204 dst_sel:DWORD dst_unused:UNUSED_PAD src0_sel:WORD_1 src1_sel:DWORD
	v_and_b32_sdwa v53, v62, v204 dst_sel:DWORD dst_unused:UNUSED_PAD src0_sel:WORD_1 src1_sel:DWORD
	v_add3_u32 v59, v59, v60, s2
	v_add3_u32 v58, v58, v61, s2
	v_add3_u32 v53, v62, v53, s2
	v_add3_u32 v51, v63, v51, s2
	v_and_b32_e32 v59, 0xffff0000, v59
	v_and_b32_e32 v58, 0xffff0000, v58
	v_or_b32_sdwa v59, v59, v51 dst_sel:DWORD dst_unused:UNUSED_PAD src0_sel:DWORD src1_sel:WORD_1
	v_or_b32_sdwa v58, v58, v53 dst_sel:DWORD dst_unused:UNUSED_PAD src0_sel:DWORD src1_sel:WORD_1
	global_store_dwordx2 v[76:77], v[58:59], off offset:2208
	v_mov_b32_e32 v59, v54
	v_mov_b32_e32 v54, v57
	v_mov_b32_e32 v58, v56
	v_pk_mul_f32 v[54:55], v[54:55], v[74:75] op_sel_hi:[1,0]
	v_and_b32_e32 v57, 0xffff0000, v133
	v_and_b32_e32 v56, 0xffff0000, v132
	v_pk_mul_f32 v[58:59], v[58:59], v[74:75] op_sel_hi:[1,0]
	v_lshlrev_b32_e32 v61, 16, v133
	v_lshlrev_b32_e32 v60, 16, v132
	v_pk_mul_f32 v[54:55], v[54:55], v[56:57]
	v_pk_mul_f32 v[58:59], v[58:59], v[60:61]
	v_and_b32_sdwa v57, v54, v204 dst_sel:DWORD dst_unused:UNUSED_PAD src0_sel:WORD_1 src1_sel:DWORD
	v_and_b32_sdwa v53, v58, v204 dst_sel:DWORD dst_unused:UNUSED_PAD src0_sel:WORD_1 src1_sel:DWORD
	v_and_b32_sdwa v56, v55, v204 dst_sel:DWORD dst_unused:UNUSED_PAD src0_sel:WORD_1 src1_sel:DWORD
	v_add3_u32 v54, v54, v57, s2
	v_and_b32_sdwa v51, v59, v204 dst_sel:DWORD dst_unused:UNUSED_PAD src0_sel:WORD_1 src1_sel:DWORD
	v_add3_u32 v53, v58, v53, s2
	v_add3_u32 v55, v55, v56, s2
	v_and_b32_e32 v54, 0xffff0000, v54
	v_add3_u32 v51, v59, v51, s2
	v_and_b32_e32 v55, 0xffff0000, v55
	v_or_b32_sdwa v54, v54, v53 dst_sel:DWORD dst_unused:UNUSED_PAD src0_sel:DWORD src1_sel:WORD_1
	v_mov_b32_e32 v53, v50
	v_or_b32_sdwa v55, v55, v51 dst_sel:DWORD dst_unused:UNUSED_PAD src0_sel:DWORD src1_sel:WORD_1
	v_pk_mul_f32 v[50:51], v[52:53], v[74:75] op_sel_hi:[1,0]
	v_lshlrev_b32_e32 v53, 16, v131
	v_lshlrev_b32_e32 v52, 16, v130
	global_store_dwordx2 v[76:77], v[54:55], off offset:2240
	v_pk_mul_f32 v[50:51], v[50:51], v[52:53]
	v_pk_mul_f32 v[52:53], v[66:67], v[74:75] op_sel_hi:[1,0]
	v_and_b32_e32 v55, 0xffff0000, v131
	v_and_b32_e32 v54, 0xffff0000, v130
	v_pk_mul_f32 v[52:53], v[52:53], v[54:55]
	v_and_b32_sdwa v54, v51, v204 dst_sel:DWORD dst_unused:UNUSED_PAD src0_sel:WORD_1 src1_sel:DWORD
	v_and_b32_sdwa v55, v50, v204 dst_sel:DWORD dst_unused:UNUSED_PAD src0_sel:WORD_1 src1_sel:DWORD
	v_add3_u32 v50, v50, v55, s2
	v_add3_u32 v51, v51, v54, s2
	v_and_b32_sdwa v54, v53, v204 dst_sel:DWORD dst_unused:UNUSED_PAD src0_sel:WORD_1 src1_sel:DWORD
	v_and_b32_sdwa v55, v52, v204 dst_sel:DWORD dst_unused:UNUSED_PAD src0_sel:WORD_1 src1_sel:DWORD
	v_add3_u32 v53, v53, v54, s2
	v_add3_u32 v52, v52, v55, s2
	v_and_b32_e32 v53, 0xffff0000, v53
	v_and_b32_e32 v52, 0xffff0000, v52
	v_or_b32_sdwa v51, v53, v51 dst_sel:DWORD dst_unused:UNUSED_PAD src0_sel:DWORD src1_sel:WORD_1
	v_or_b32_sdwa v50, v52, v50 dst_sel:DWORD dst_unused:UNUSED_PAD src0_sel:DWORD src1_sel:WORD_1
	global_store_dwordx2 v[76:77], v[50:51], off offset:2272
	s_waitcnt vmcnt(7)
	v_mov_b64_e32 v[64:65], v[36:37]
	v_mov_b64_e32 v[60:61], v[40:41]
	v_mov_b64_e32 v[56:57], v[44:45]
	v_mov_b64_e32 v[52:53], v[48:49]
	s_andn2_b64 vcc, exec, s[30:31]
	v_mov_b64_e32 v[62:63], v[34:35]
	v_mov_b64_e32 v[58:59], v[38:39]
	v_mov_b64_e32 v[54:55], v[42:43]
	v_mov_b64_e32 v[50:51], v[46:47]
	global_store_dwordx2 v[76:77], v[70:71], off offset:2144
	s_barrier
	s_cbranch_vccnz .LBB0_656
	v_readlane_b32 s54, v252, 54
	v_readlane_b32 s80, v252, 45
	v_readlane_b32 s90, v252, 43
	v_readlane_b32 s95, v252, 53
	v_readlane_b32 s55, v252, 55
	v_readlane_b32 s81, v252, 46
	v_readlane_b32 s91, v252, 44
